# speedup vs baseline: 1.0177x; 1.0177x over previous
.LBB1_13:
.LBB1_14:
	ds_read_b32 v4, v4 offset:34816
	s_waitcnt lgkmcnt(1)
	v_lshrrev_b32_e32 v7, 5, v8
	v_lshlrev_b32_e64 v9, v8, 1
	v_cmp_eq_u32_e32 vcc, v3, v7
	v_lshl_add_u32 v10, 2, v8, -1
	v_readfirstlane_b32 s3, v7
	s_add_i32 s43, s3, 1
	s_cmp_lt_u32 s3, 15
	s_cselect_b32 s41, s43, 15
	v_readlane_b32 s42, v6, s41
	s_cselect_b32 s42, s42, 0
	v_cndmask_b32_e32 v9, 0, v9, vcc
	v_cndmask_b32_e32 v10, 0, v10, vcc
	v_cmp_ge_u32_e32 vcc, v3, v7
	v_or_b32_e32 v16, v6, v9
	s_movk_i32 s15, 0x410
	v_cndmask_b32_e32 v10, -1, v10, vcc
	s_waitcnt lgkmcnt(0)
	v_and_b32_e32 v4, v4, v10
	v_cmp_le_u32_e32 vcc, v3, v7
	v_and_b32_e32 v2, 63, v0
	s_nop 0
	v_cndmask_b32_e32 v4, -1, v4, vcc
	v_cmp_ne_u32_e32 vcc, s43, v3
	s_nop 1
	v_cndmask_b32_e32 v4, 0, v4, vcc
	v_bitop3_b32 v4, v4, v6, v9 bitop3:0xe0
	v_bitop3_b32 v6, v6, v10, v9 bitop3:0x32
	v_bcnt_u32_b32 v12, v4, 0
	v_readlane_b32 s3, v6, s3
	v_bcnt_u32_b32 v6, v16, 0
	v_lshlrev_b32_e32 v13, 16, v6
	v_or_b32_e32 v6, v12, v13
	v_mov_b32_e32 v9, 0
	v_mov_b64_e32 v[10:11], s[10:11]
	v_mov_b32_dpp v17, v6 row_shr:1 row_mask:0xf bank_mask:0xf bound_ctrl:1
	v_add_u32_e32 v6, v6, v17
	v_cmp_gt_u32_e32 vcc, 16, v2
	s_nop 0
	v_mov_b32_dpp v18, v6 row_shr:2 row_mask:0xf bank_mask:0xf bound_ctrl:1
	v_add_u32_e32 v6, v6, v18
	s_nop 1
	v_mov_b32_dpp v19, v6 row_shr:4 row_mask:0xf bank_mask:0xf bound_ctrl:1
	v_add_u32_e32 v6, v6, v19
	s_nop 1
	v_mov_b32_dpp v20, v6 row_shr:8 row_mask:0xf bank_mask:0xf bound_ctrl:1
	v_add_u32_e32 v21, v6, v20
	v_lshl_add_u64 v[6:7], s[4:5], 0, v[8:9]
	v_mad_u64_u32 v[10:11], s[4:5], v6, s15, v[10:11]
	v_cmp_ne_u32_e64 s[4:5], 0, v4
	v_readlane_b32 s18, v21, 15
	v_mad_u32_u24 v11, v7, s15, v11
	s_and_b64 s[10:11], vcc, s[4:5]
	s_and_saveexec_b64 s[4:5], s[10:11]
	s_cbranch_execz .LBB1_21
	v_mul_hi_u32_u24_e32 v23, 48, v8
	v_mul_u32_u24_e32 v22, 48, v8
	v_mov_b32_e32 v8, 0x6000
	v_mad_u64_u32 v[22:23], s[10:11], s14, v8, v[22:23]
	v_add_u32_e32 v8, v17, v18
	v_add3_u32 v8, v8, v19, v20
	v_add3_u32 v8, v8, v12, v13
	v_sub_u32_sdwa v21, v21, v12 dst_sel:DWORD dst_unused:UNUSED_PAD src0_sel:WORD_0 src1_sel:DWORD
	v_sub_u32_sdwa v12, v8, v12 dst_sel:DWORD dst_unused:UNUSED_PAD src0_sel:WORD_0 src1_sel:DWORD
	v_ashrrev_i32_e32 v13, 31, v12
	v_lshl_add_u64 v[12:13], v[12:13], 1, v[22:23]
	v_lshlrev_b32_e32 v3, 5, v3
	v_lshl_add_u64 v[12:13], s[8:9], 0, v[12:13]
	s_mov_b64 s[10:11], 0
	v_mov_b32_e32 v8, v21
	s_branch .LBB1_17

.LBB1_25:
	s_or_b64 exec, exec, s[4:5]
	v_cmp_eq_u32_e32 vcc, 0, v2
	s_and_saveexec_b64 s[4:5], vcc
	s_cbranch_execz .LBB1_27
	v_lshl_add_u64 v[6:7], v[6:7], 4, s[12:13]
	v_mov_b32_e32 v2, s10
	v_mov_b32_e32 v3, s3
	s_waitcnt vmcnt(8)
	v_lshl_or_b32 v2, v5, 16, v2
	v_mov_b32_e32 v5, s42
	global_store_dwordx4 v[6:7], v[2:5], off

	.amdhsa_kernel _Z7k2_elimPKjPKiPiS2_PfP15HIP_vector_typeIiLj4EEPKfS4_PtSA_
		.amdhsa_group_segment_fixed_size 34880
		.amdhsa_private_segment_fixed_size 0
		.amdhsa_kernarg_size 80
		.amdhsa_user_sgpr_count 2
		.amdhsa_user_sgpr_dispatch_ptr 0
		.amdhsa_user_sgpr_queue_ptr 0
		.amdhsa_user_sgpr_kernarg_segment_ptr 1
		.amdhsa_user_sgpr_dispatch_id 0
		.amdhsa_user_sgpr_kernarg_preload_length 0
		.amdhsa_user_sgpr_kernarg_preload_offset 0
		.amdhsa_user_sgpr_private_segment_size 0
		.amdhsa_uses_dynamic_stack 0
		.amdhsa_enable_private_segment 0
		.amdhsa_system_sgpr_workgroup_id_x 1
		.amdhsa_system_sgpr_workgroup_id_y 0
		.amdhsa_system_sgpr_workgroup_id_z 0
		.amdhsa_system_sgpr_workgroup_info 0
		.amdhsa_system_vgpr_workitem_id 0
		.amdhsa_next_free_vgpr 35
		.amdhsa_next_free_sgpr 44
		.amdhsa_accum_offset 36
		.amdhsa_reserve_vcc 1
		.amdhsa_float_round_mode_32 0
		.amdhsa_float_round_mode_16_64 0
		.amdhsa_float_denorm_mode_32 3
		.amdhsa_float_denorm_mode_16_64 3
		.amdhsa_dx10_clamp 1
		.amdhsa_ieee_mode 1
		.amdhsa_fp16_overflow 0
		.amdhsa_tg_split 0
		.amdhsa_exception_fp_ieee_invalid_op 0
		.amdhsa_exception_fp_denorm_src 0
		.amdhsa_exception_fp_ieee_div_zero 0
		.amdhsa_exception_fp_ieee_overflow 0
		.amdhsa_exception_fp_ieee_underflow 0
		.amdhsa_exception_fp_ieee_inexact 0
		.amdhsa_exception_int_div_zero 0
	.end_amdhsa_kernel

_Z8k3_chainPKfPK15HIP_vector_typeIiLj4EEPKtS6_S0_S0_Pf:
	s_load_dwordx8 s[8:15], s[0:1], 0x0
	s_load_dwordx4 s[4:7], s[0:1], 0x20
	s_load_dwordx2 s[16:17], s[0:1], 0x30
	s_mul_hi_u32 s0, s2, 0xaaaaaaab
	s_lshr_b32 s20, s0, 5
	s_mul_i32 s0, s20, 48
	s_mov_b32 s21, 0
	s_sub_i32 s18, s2, s0
	s_lshl_b64 s[0:1], s[20:21], 13
	s_waitcnt lgkmcnt(0)
	s_add_u32 s2, s10, s0
	v_and_b32_e32 v1, 3, v0
	s_addc_u32 s3, s11, s1
	s_mul_hi_u32 s1, s20, 0x18000
	s_mul_i32 s0, s20, 0x18000
	v_lshlrev_b32_e32 v104, 4, v0
	v_mov_b32_e32 v105, 0
	v_lshl_or_b32 v98, s18, 2, v1
	s_lshl_b64 s[18:19], s[0:1], 4
	v_lshl_add_u64 v[2:3], s[2:3], 0, v[104:105]
	s_add_u32 s0, s8, s18
	s_movk_i32 s8, 0x1000
	v_add_co_u32_e32 v10, vcc, s8, v2
	s_addc_u32 s1, s9, s19
	s_nop 0
	v_addc_co_u32_e32 v11, vcc, 0, v3, vcc
	global_load_dwordx4 v[2:5], v104, s[2:3]
	global_load_dwordx4 v[6:9], v[10:11], off
	s_mul_i32 s2, s20, 0x6000
	s_mul_hi_u32 s3, s20, 0x6000
	s_add_u32 s2, s12, s2
	s_addc_u32 s3, s13, s3
	v_lshl_add_u64 v[10:11], s[2:3], 0, v[104:105]
	s_movk_i32 s8, 0x2000
	v_add_co_u32_e32 v12, vcc, s8, v10
	s_movk_i32 s8, 0x3000
	s_nop 0
	v_addc_co_u32_e32 v13, vcc, 0, v11, vcc
	global_load_dwordx4 v[38:41], v104, s[2:3]
	global_load_dwordx4 v[42:45], v[12:13], off offset:-4096
	global_load_dwordx4 v[46:49], v[12:13], off
	v_add_co_u32_e32 v12, vcc, s8, v10
	v_lshrrev_b32_e32 v110, 2, v0
	s_nop 0
	v_addc_co_u32_e32 v13, vcc, 0, v11, vcc
	v_or_b32_e32 v14, 0x4000, v104
	global_load_dwordx4 v[50:53], v[12:13], off
	global_load_dwordx4 v[54:57], v14, s[2:3]
	s_movk_i32 s2, 0x5000
	v_add_co_u32_e32 v10, vcc, s2, v10
	s_movk_i32 s2, 0xc0
	v_or_b32_e32 v18, 64, v110
	v_addc_co_u32_e32 v11, vcc, 0, v11, vcc
	v_mov_b32_e32 v99, v105
	v_mad_u32_u24 v106, v110, s2, v98
	v_mov_b32_e32 v107, v105
	v_mul_u32_u24_e32 v102, 0xc00, v18
	v_mov_b32_e32 v103, v105
	global_load_dwordx4 v[66:69], v[10:11], off
	v_lshlrev_b64 v[10:11], 4, v[106:107]
	v_lshl_add_u64 v[14:15], s[0:1], 0, v[102:103]
	v_lshlrev_b64 v[16:17], 4, v[98:99]
	v_lshl_add_u64 v[12:13], s[0:1], 0, v[10:11]
	v_lshl_add_u64 v[14:15], v[14:15], 0, v[16:17]
	s_mov_b32 s3, 0x30000
	global_load_dwordx4 v[58:61], v[12:13], off
	global_load_dwordx4 v[62:65], v[14:15], off
	v_add_co_u32_e32 v12, vcc, s3, v14
	s_mov_b32 s3, 0x60000
	s_nop 0
	v_addc_co_u32_e32 v13, vcc, 0, v15, vcc
	v_add_co_u32_e32 v14, vcc, s3, v14
	s_movk_i32 s2, 0xc00
	s_nop 0
	v_addc_co_u32_e32 v15, vcc, 0, v15, vcc
	global_load_dwordx4 v[70:73], v[12:13], off
	global_load_dwordx4 v[74:77], v[14:15], off
	v_mov_b32_e32 v12, 0x90000
	v_mad_u32_u24 v12, v18, s2, v12
	v_mov_b32_e32 v13, v105
	v_mov_b32_e32 v14, 0xc0000
	v_lshl_add_u64 v[12:13], s[0:1], 0, v[12:13]
	v_mad_u32_u24 v100, v18, s2, v14
	v_mov_b32_e32 v101, v105
	v_lshl_add_u64 v[12:13], v[12:13], 0, v[16:17]
	v_lshl_add_u64 v[14:15], s[0:1], 0, v[100:101]
	v_lshl_add_u64 v[14:15], v[14:15], 0, v[16:17]
	global_load_dwordx4 v[78:81], v[12:13], off
	global_load_dwordx4 v[82:85], v[14:15], off
	v_mov_b32_e32 v12, 0xf0000
	v_mad_u32_u24 v96, v18, s2, v12
	v_mov_b32_e32 v97, v105
	v_mov_b32_e32 v14, 0x120000
	v_lshl_add_u64 v[12:13], s[0:1], 0, v[96:97]
	v_mad_u32_u24 v94, v18, s2, v14
	v_mov_b32_e32 v95, v105
	v_lshl_add_u64 v[12:13], v[12:13], 0, v[16:17]
	v_lshl_add_u64 v[14:15], s[0:1], 0, v[94:95]
	v_lshl_add_u64 v[14:15], v[14:15], 0, v[16:17]
	global_load_dwordx4 v[86:89], v[12:13], off
	global_load_dwordx4 v[90:93], v[14:15], off
	s_waitcnt vmcnt(15)
	ds_write_b128 v104, v[2:5] offset:57408
	s_waitcnt vmcnt(14)
	ds_write_b128 v104, v[6:9] offset:61504
	v_lshl_add_u64 v[2:3], s[6:7], 0, v[10:11]
	s_waitcnt lgkmcnt(0)
	s_barrier
	global_load_dwordx4 v[34:37], v[2:3], off
	v_lshl_add_u64 v[2:3], s[4:5], 0, v[10:11]
	v_add_u32_e32 v4, 0x3000, v106
	v_mov_b32_e32 v5, v105
	v_lshl_add_u64 v[4:5], v[4:5], 4, s[4:5]
	global_load_dwordx4 v[30:33], v[2:3], off
	global_load_dwordx4 v[26:29], v[4:5], off
	v_add_u32_e32 v2, 0x6000, v106
	v_mov_b32_e32 v3, v105
	v_lshl_add_u64 v[2:3], v[2:3], 4, s[4:5]
	v_add_u32_e32 v4, 0x9000, v106
	v_mov_b32_e32 v5, v105
	v_lshl_add_u64 v[4:5], v[4:5], 4, s[4:5]
	global_load_dwordx4 v[22:25], v[2:3], off
	global_load_dwordx4 v[18:21], v[4:5], off
	v_add_u32_e32 v2, 0xc000, v106
	v_mov_b32_e32 v3, v105
	v_lshl_add_u64 v[2:3], v[2:3], 4, s[4:5]
	v_add_u32_e32 v4, 0xf000, v106
	v_mov_b32_e32 v5, v105
	v_lshl_add_u64 v[4:5], v[4:5], 4, s[4:5]
	global_load_dwordx4 v[14:17], v[2:3], off
	global_load_dwordx4 v[10:13], v[4:5], off
	v_add_u32_e32 v2, 0x12000, v106
	v_mov_b32_e32 v3, v105
	v_lshl_add_u64 v[108:109], v[2:3], 4, s[4:5]
	v_add_u32_e32 v2, 0x15000, v106
	v_lshl_add_u64 v[106:107], v[2:3], 4, s[4:5]
	global_load_dwordx4 v[6:9], v[108:109], off
	global_load_dwordx4 v[2:5], v[106:107], off
	v_bfe_u32 v113, v0, 5, 1
	v_lshrrev_b32_e32 v115, 6, v0
	v_lshlrev_b32_e32 v112, 2, v113
	v_and_b32_e32 v111, 31, v0
	v_or_b32_e32 v116, v112, v115
	v_lshl_or_b32 v120, v116, 5, v111
	v_lshlrev_b32_e32 v108, 4, v120
	ds_read_b32 v140, v108 offset:57420
	ds_read_b32 v141, v108 offset:61516
	v_lshlrev_b32_e32 v142, 9, v116
	v_add_u32_e32 v142, 0x200, v142
	v_add_u32_e32 v143, 0x1000, v142
	v_mov_b32_e32 v152, 0x2000
	s_waitcnt lgkmcnt(0)
	v_ffbl_b32_e32 v153, v140
	v_ffbl_b32_e32 v154, v141
	v_cmp_ne_u32_e32 vcc, 0, v140
	v_cmp_ne_u32_e64 s[22:23], 0, v141
	v_lshl_add_u32 v153, v153, 4, v142
	v_lshl_add_u32 v154, v154, 4, v143
	v_cndmask_b32_e32 v144, v152, v153, vcc
	v_cndmask_b32_e64 v148, v152, v154, s[22:23]
	v_add_u32_e32 v153, -1, v140
	v_add_u32_e32 v154, -1, v141
	v_and_b32_e32 v140, v153, v140
	v_and_b32_e32 v141, v154, v141
	v_ffbl_b32_e32 v153, v140
	v_ffbl_b32_e32 v154, v141
	v_cmp_ne_u32_e32 vcc, 0, v140
	v_cmp_ne_u32_e64 s[22:23], 0, v141
	v_lshl_add_u32 v153, v153, 4, v142
	v_lshl_add_u32 v154, v154, 4, v143
	v_cndmask_b32_e32 v145, v152, v153, vcc
	v_cndmask_b32_e64 v149, v152, v154, s[22:23]
	v_add_u32_e32 v153, -1, v140
	v_add_u32_e32 v154, -1, v141
	v_and_b32_e32 v140, v153, v140
	v_and_b32_e32 v141, v154, v141
	v_ffbl_b32_e32 v153, v140
	v_ffbl_b32_e32 v154, v141
	v_cmp_ne_u32_e32 vcc, 0, v140
	v_cmp_ne_u32_e64 s[22:23], 0, v141
	v_lshl_add_u32 v153, v153, 4, v142
	v_lshl_add_u32 v154, v154, 4, v143
	v_cndmask_b32_e32 v146, v152, v153, vcc
	v_cndmask_b32_e64 v150, v152, v154, s[22:23]
	v_add_u32_e32 v153, -1, v140
	v_add_u32_e32 v154, -1, v141
	v_and_b32_e32 v140, v153, v140
	v_and_b32_e32 v141, v154, v141
	v_ffbl_b32_e32 v153, v140
	v_ffbl_b32_e32 v154, v141
	v_cmp_ne_u32_e32 vcc, 0, v140
	v_cmp_ne_u32_e64 s[22:23], 0, v141
	v_lshl_add_u32 v153, v153, 4, v142
	v_lshl_add_u32 v154, v154, 4, v143
	v_cndmask_b32_e32 v147, v152, v153, vcc
	v_cndmask_b32_e64 v151, v152, v154, s[22:23]
	v_add_u32_e32 v153, -1, v140
	v_add_u32_e32 v154, -1, v141
	v_and_b32_e32 v140, v153, v140
	v_and_b32_e32 v141, v154, v141
	v_lshl_or_b32 v144, v145, 16, v144
	v_lshl_or_b32 v145, v147, 16, v146
	v_lshl_or_b32 v148, v149, 16, v148
	v_lshl_or_b32 v149, v151, 16, v150
	v_lshrrev_b32_e32 v153, 1, v108
	v_add_u32_e32 v153, 0x118c0, v153
	v_lshrrev_b32_e32 v154, 2, v108
	v_add_u32_e32 v154, 0x128c0, v154
	ds_write_b64 v153, v[144:145]
	ds_write_b64 v153, v[148:149] offset:2048
	ds_write_b32 v154, v140
	ds_write_b32 v154, v141 offset:1024
	v_cmp_ne_u32_e32 vcc, 0, v140
	v_cmp_ne_u32_e64 s[22:23], 0, v141
	v_lshlrev_b32_e32 v150, 5, v113
	v_lshlrev_b32_e32 v155, 2, v116
	v_add_u32_e32 v155, 0x11880, v155
	v_lshrrev_b64 v[146:147], v150, vcc
	v_lshrrev_b64 v[156:157], v150, s[22:23]
	v_mov_b32_e32 v151, 0x400
	v_cmp_ne_u32_e32 vcc, 0, v146
	v_cmp_ne_u32_e64 s[22:23], 0, v156
	s_nop 1
	v_cndmask_b32_e32 v146, 0, v151, vcc
	v_cndmask_b32_e64 v156, 0, v151, s[22:23]
	v_cmp_eq_u32_e32 vcc, 0, v111
	s_and_saveexec_b64 s[22:23], vcc
	ds_write_b32 v155, v146
	ds_write_b32 v155, v156 offset:32
	s_or_b64 exec, exec, s[22:23]
	ds_read_b64 v[106:107], v108 offset:57408
	ds_read_u16 v118, v108 offset:57410
	v_and_b32_e32 v114, 63, v0
	v_and_b32_e32 v0, 32, v0
	v_add_u32_e32 v117, 0xe040, v108
	v_mov_b32_e32 v108, -1
	v_mov_b32_e32 v119, v105
	s_branch .LBB2_2

.LBB2_6:
	s_or_b64 exec, exec, s[12:13]
	v_lshlrev_b32_e32 v105, 9, v116
	v_ffbl_b32_e32 v106, v107
	v_ffbl_b32_e32 v109, v109
	v_lshlrev_b32_e32 v120, 25, v116
	v_lshl_or_b32 v106, v106, 4, v105
	v_mov_b32_e32 v107, 0x2000
	v_lshl_or_b32 v109, v109, 20, v120
	v_bfrev_b32_e32 v120, 4
	v_cndmask_b32_e64 v106, v106, v107, s[8:9]
	v_cndmask_b32_e64 v109, v109, v120, s[4:5]
	v_ffbl_b32_e32 v108, v108
	v_lshl_or_b32 v105, v108, 4, v105
	v_or_b32_e32 v108, v109, v106
	v_lshlrev_b32_e32 v106, 16, v119
	v_or_b32_e32 v119, 8, v116
	v_cndmask_b32_e32 v105, v105, v107, vcc
	v_mov_b32_e32 v107, 0x800000
	v_lshl_or_b32 v121, v119, 5, v111
	v_cndmask_b32_e64 v107, 0, v107, s[6:7]
	s_waitcnt lgkmcnt(1)
	v_lshl_or_b32 v105, v118, 24, v105
	v_lshlrev_b32_e32 v109, 4, v121
	v_or3_b32 v105, v105, v107, v106
	ds_read_b64 v[106:107], v109 offset:57408
	ds_read_u16 v118, v109 offset:57410
	v_mov_b32_e32 v120, 0
	ds_write2_b32 v117, v108, v105 offset0:1 offset1:3
	v_add_u32_e32 v105, 0xe040, v109
	v_mov_b32_e32 v108, -1
	v_mov_b32_e32 v117, 0
	s_branch .LBB2_8

.LBB2_12:
	s_or_b64 exec, exec, s[12:13]
	v_lshlrev_b32_e32 v106, 9, v119
	v_ffbl_b32_e32 v107, v107
	v_ffbl_b32_e32 v108, v108
	v_lshlrev_b32_e32 v116, 25, v119
	v_lshl_or_b32 v107, v107, 4, v106
	v_mov_b32_e32 v109, 0x2000
	v_lshl_or_b32 v108, v108, 20, v116
	v_bfrev_b32_e32 v116, 4
	v_ffbl_b32_e32 v0, v0
	v_cndmask_b32_e64 v107, v107, v109, s[8:9]
	v_cndmask_b32_e64 v108, v108, v116, s[4:5]
	v_lshl_or_b32 v0, v0, 4, v106
	v_cndmask_b32_e32 v0, v0, v109, vcc
	v_or_b32_e32 v106, v108, v107
	v_mov_b32_e32 v108, 0x800000
	v_lshlrev_b32_e32 v107, 16, v117
	v_cndmask_b32_e64 v108, 0, v108, s[6:7]
	s_waitcnt lgkmcnt(2)
	v_lshl_or_b32 v0, v118, 24, v0
	v_or3_b32 v0, v0, v108, v107
	ds_write2_b32 v105, v106, v0 offset0:1 offset1:3
	s_movk_i32 s2, 0x2010
	v_mul_u32_u24_e32 v105, 0x2010, v115
	v_cmp_eq_u32_e32 vcc, 0, v114
	s_waitcnt vmcnt(22)
	ds_write_b128 v104, v[38:41] offset:32832
	s_waitcnt vmcnt(21)
	ds_write_b128 v104, v[42:45] offset:36928
	s_waitcnt vmcnt(20)
	ds_write_b128 v104, v[46:49] offset:41024
	s_waitcnt vmcnt(19)
	ds_write_b128 v104, v[50:53] offset:45120
	s_waitcnt vmcnt(18)
	ds_write_b128 v104, v[54:57] offset:49216
	s_waitcnt vmcnt(17)
	ds_write_b128 v104, v[66:69] offset:53312
	s_and_saveexec_b64 s[0:1], vcc
	v_mov_b32_e32 v38, 0
	v_mov_b32_e32 v39, v38
	v_mov_b32_e32 v40, v38
	v_mov_b32_e32 v41, v38
	ds_write_b128 v105, v[38:41] offset:8192
	s_or_b64 exec, exec, s[0:1]
	v_lshlrev_b32_e32 v40, 3, v113
	v_lshlrev_b32_e32 v67, 4, v110
	v_or_b32_e32 v38, 0x1e0, v111
	v_or_b32_e32 v0, 0x8040, v40
	v_mad_u32_u24 v66, v1, s2, v67
	v_mad_u32_u24 v38, v38, 48, v0
	s_waitcnt vmcnt(16)
	ds_write_b128 v66, v[58:61]
	s_waitcnt vmcnt(15)
	ds_write_b128 v66, v[62:65] offset:1024
	s_waitcnt vmcnt(14)
	ds_write_b128 v66, v[70:73] offset:2048
	s_waitcnt vmcnt(13)
	ds_write_b128 v66, v[74:77] offset:3072
	s_waitcnt vmcnt(12)
	ds_write_b128 v66, v[78:81] offset:4096
	s_waitcnt vmcnt(11)
	ds_write_b128 v66, v[82:85] offset:5120
	s_waitcnt vmcnt(10)
	ds_write_b128 v66, v[86:89] offset:6144
	s_waitcnt vmcnt(9)
	ds_write_b128 v66, v[90:93] offset:7168
	s_waitcnt lgkmcnt(0)
	s_barrier
	v_lshl_add_u32 v116, v113, 3, v105
	v_or_b32_e32 v106, 0x1e0, v111
	v_lshlrev_b32_e32 v138, 4, v106
	v_lshlrev_b32_e32 v139, 3, v106
	v_add_u32_e32 v139, 0x118c0, v139
	v_mul_u32_u24_e32 v156, 48, v106
	v_add_u32_e32 v156, v0, v156
	v_mov_b32_e32 v157, 0x1187c
	v_add_u32_e32 v137, v116, v138
	v_lshlrev_b32_e32 v160, 4, v111
	v_lshlrev_b32_e32 v161, 3, v111
	v_add_u32_e32 v161, 0x118c0, v161
	v_mul_u32_u24_e32 v162, 48, v111
	v_add_u32_e32 v162, v0, v162
	v_mov_b32_e32 v163, 0x11840
	v_mul_hi_u32_u24_e32 v159, 0x410, v111
	v_mul_u32_u24_e32 v158, 0x410, v111
	v_mov_b32_e32 v107, 0x82000
	v_mad_u64_u32 v[158:159], s[0:1], s20, v107, v[158:159]
	v_lshlrev_b32_e32 v107, 3, v113
	v_or_b32_e32 v158, v158, v107
	v_lshl_add_u64 v[158:159], s[14:15], 0, v[158:159]
	s_mov_b64 s[0:1], 0x79e30
	s_mov_b32 s2, 0xffff7e00
	s_mov_b32 s3, -1
	v_lshl_add_u64 v[158:159], v[158:159], 0, s[0:1]
	ds_read_b128 v[38:41], v138 offset:57408
	ds_read_b64 v[42:43], v139
	ds_read2_b64 v[56:59], v156 offset1:2
	ds_read2_b32 v[60:61], v157 offset1:16
	v_add_u32_e32 v156, 0xfffffa00, v156
	v_add_u32_e32 v157, -4, v157
	ds_read2_b64 v[52:55], v156 offset1:2
	ds_read2_b32 v[64:65], v157 offset1:16
	s_waitcnt lgkmcnt(0)
	v_or_b32_e32 v60, v60, v61
	v_or_b32_e32 v64, v64, v65
	s_nop 0
	v_readfirstlane_b32 s4, v60
	v_readfirstlane_b32 s21, v64
	v_add_u32_sdwa v92, v105, v56 dst_sel:DWORD dst_unused:UNUSED_PAD src0_sel:DWORD src1_sel:WORD_0
	v_add_u32_sdwa v93, v105, v56 dst_sel:DWORD dst_unused:UNUSED_PAD src0_sel:DWORD src1_sel:WORD_1
	v_add_u32_sdwa v106, v105, v57 dst_sel:DWORD dst_unused:UNUSED_PAD src0_sel:DWORD src1_sel:WORD_0
	v_add_u32_sdwa v107, v105, v57 dst_sel:DWORD dst_unused:UNUSED_PAD src0_sel:DWORD src1_sel:WORD_1
	v_add_u32_sdwa v108, v105, v58 dst_sel:DWORD dst_unused:UNUSED_PAD src0_sel:DWORD src1_sel:WORD_0
	v_add_u32_sdwa v109, v105, v58 dst_sel:DWORD dst_unused:UNUSED_PAD src0_sel:DWORD src1_sel:WORD_1
	v_add_u32_sdwa v88, v105, v59 dst_sel:DWORD dst_unused:UNUSED_PAD src0_sel:DWORD src1_sel:WORD_0
	v_add_u32_sdwa v89, v105, v59 dst_sel:DWORD dst_unused:UNUSED_PAD src0_sel:DWORD src1_sel:WORD_1
	ds_read_b128 v[120:123], v92
	ds_read_b128 v[124:127], v93
	ds_read_b128 v[128:131], v106
	ds_read_b128 v[132:135], v107
	ds_read_b128 v[140:143], v108
	ds_read_b128 v[144:147], v109
	ds_read_b128 v[148:151], v88
	ds_read_b128 v[152:155], v89
	s_waitcnt lgkmcnt(0)
	v_pk_add_f32 v[120:121], v[120:121], v[124:125]
	v_pk_add_f32 v[122:123], v[122:123], v[126:127]
	v_pk_add_f32 v[128:129], v[128:129], v[132:133]
	v_pk_add_f32 v[130:131], v[130:131], v[134:135]
	v_pk_add_f32 v[140:141], v[140:141], v[144:145]
	v_pk_add_f32 v[142:143], v[142:143], v[146:147]
	v_pk_add_f32 v[148:149], v[148:149], v[152:153]
	v_pk_add_f32 v[150:151], v[150:151], v[154:155]
	s_bitcmp1_b32 s4, 8
	s_cbranch_scc1 .Lfarslow_pre
.Lfarslow_ret_pre:
	v_pk_add_f32 v[120:121], v[120:121], v[128:129]
	v_pk_add_f32 v[122:123], v[122:123], v[130:131]
	v_pk_add_f32 v[140:141], v[140:141], v[148:149]
	v_pk_add_f32 v[142:143], v[142:143], v[150:151]
	v_pk_add_f32 v[120:121], v[120:121], v[140:141]
	v_pk_add_f32 v[122:123], v[122:123], v[142:143]
	s_nop 1
	v_permlane32_swap_b32_e32 v120, v122
	v_permlane32_swap_b32_e32 v121, v123
	v_pk_add_f32 v[44:45], v[120:121], v[122:123]
	v_add_u32_e32 v138, 0xfffffe00, v138
	v_add_u32_e32 v139, 0xffffff00, v139
	v_add_u32_e32 v156, 0xfffffa00, v156
	v_add_u32_e32 v157, -4, v157
	v_lshl_add_u64 v[158:159], v[158:159], 0, s[2:3]
	s_mov_b32 s5, 15
.Lchain_top:
.Lit_A:
	v_add_u32_sdwa v88, v116, v42 dst_sel:DWORD dst_unused:UNUSED_PAD src0_sel:DWORD src1_sel:WORD_0
	v_add_u32_sdwa v89, v116, v42 dst_sel:DWORD dst_unused:UNUSED_PAD src0_sel:DWORD src1_sel:WORD_1
	ds_read_b64 v[68:69], v88
	v_add_u32_sdwa v90, v116, v43 dst_sel:DWORD dst_unused:UNUSED_PAD src0_sel:DWORD src1_sel:WORD_0
	ds_read_b64 v[70:71], v89
	v_add_u32_sdwa v91, v116, v43 dst_sel:DWORD dst_unused:UNUSED_PAD src0_sel:DWORD src1_sel:WORD_1
	ds_read_b64 v[72:73], v90
	ds_read_b64 v[74:75], v91
	v_add_u32_sdwa v92, v105, v52 dst_sel:DWORD dst_unused:UNUSED_PAD src0_sel:DWORD src1_sel:WORD_0
	v_add_u32_sdwa v93, v105, v52 dst_sel:DWORD dst_unused:UNUSED_PAD src0_sel:DWORD src1_sel:WORD_1
	v_add_u32_sdwa v106, v105, v53 dst_sel:DWORD dst_unused:UNUSED_PAD src0_sel:DWORD src1_sel:WORD_0
	v_add_u32_sdwa v107, v105, v53 dst_sel:DWORD dst_unused:UNUSED_PAD src0_sel:DWORD src1_sel:WORD_1
	v_add_u32_sdwa v108, v105, v54 dst_sel:DWORD dst_unused:UNUSED_PAD src0_sel:DWORD src1_sel:WORD_0
	v_add_u32_sdwa v109, v105, v54 dst_sel:DWORD dst_unused:UNUSED_PAD src0_sel:DWORD src1_sel:WORD_1
	v_add_u32_sdwa v88, v105, v55 dst_sel:DWORD dst_unused:UNUSED_PAD src0_sel:DWORD src1_sel:WORD_0
	v_add_u32_sdwa v89, v105, v55 dst_sel:DWORD dst_unused:UNUSED_PAD src0_sel:DWORD src1_sel:WORD_1
	ds_read_b128 v[120:123], v92
	ds_read_b128 v[124:127], v93
	ds_read_b128 v[128:131], v106
	ds_read_b128 v[132:135], v107
	ds_read_b128 v[140:143], v108
	ds_read_b128 v[144:147], v109
	ds_read_b128 v[148:151], v88
	ds_read_b128 v[152:155], v89
	v_bfe_u32 v117, v41, 16, 7
	v_add_u32_sdwa v118, v116, v39 dst_sel:DWORD dst_unused:UNUSED_PAD src0_sel:DWORD src1_sel:WORD_0
	v_add_u32_sdwa v119, v116, v39 dst_sel:DWORD dst_unused:UNUSED_PAD src0_sel:DWORD src1_sel:WORD_1
	v_add_u32_sdwa v136, v116, v41 dst_sel:DWORD dst_unused:UNUSED_PAD src0_sel:DWORD src1_sel:WORD_0
	s_waitcnt lgkmcnt(11)
	v_pk_add_f32 v[76:77], v[44:45], v[68:69]
	s_waitcnt lgkmcnt(9)
	v_pk_add_f32 v[78:79], v[70:71], v[72:73]
	s_waitcnt lgkmcnt(8)
	v_pk_add_f32 v[76:77], v[76:77], v[74:75]
	s_nop 0
	v_pk_add_f32 v[76:77], v[76:77], v[78:79]
	s_bitcmp1_b32 s4, 10
	s_cbranch_scc1 .Lnearslow_A
.Lnearslow_ret_A:
	v_cmp_eq_u32_e32 vcc, 0, v117
	v_pk_mul_f32 v[78:79], v[40:41], v[76:77] op_sel_hi:[0,1]
	s_mov_b64 exec, vcc
	ds_write_b64 v137, v[78:79]
	s_mov_b64 exec, -1
	ds_read_b128 v[46:49], v138 offset:57408
	ds_read_b64 v[50:51], v139
	ds_read2_b64 v[56:59], v156 offset1:2
	ds_read2_b32 v[60:61], v157 offset1:16
	s_and_b32 s9, s4, 0xff
	s_waitcnt lgkmcnt(4)
	s_bitcmp1_b32 s4, 9
	s_cbranch_scc1 .Lfs_A
	s_cmp_eq_u32 s9, 0
	s_cbranch_scc1 .Lfs_A
	v_cmp_eq_u32_e64 s[6:7], 1, v117
	s_mov_b64 exec, s[6:7]
	ds_read_b64 v[82:83], v118
	ds_read_b64 v[84:85], v119
	ds_read_b64 v[86:87], v136
	s_mov_b64 exec, -1
.Lfs_A:
	v_pk_add_f32 v[120:121], v[120:121], v[124:125]
	v_pk_add_f32 v[122:123], v[122:123], v[126:127]
	v_pk_add_f32 v[128:129], v[128:129], v[132:133]
	v_pk_add_f32 v[130:131], v[130:131], v[134:135]
	v_pk_add_f32 v[140:141], v[140:141], v[144:145]
	v_pk_add_f32 v[142:143], v[142:143], v[146:147]
	v_pk_add_f32 v[148:149], v[148:149], v[152:153]
	v_pk_add_f32 v[150:151], v[150:151], v[154:155]
	s_bitcmp1_b32 s21, 8
	s_cbranch_scc1 .Lfarslow_A
.Lfarslow_ret_A:
	v_pk_add_f32 v[120:121], v[120:121], v[128:129]
	v_pk_add_f32 v[122:123], v[122:123], v[130:131]
	v_pk_add_f32 v[140:141], v[140:141], v[148:149]
	v_pk_add_f32 v[142:143], v[142:143], v[150:151]
	v_pk_add_f32 v[120:121], v[120:121], v[140:141]
	v_pk_add_f32 v[122:123], v[122:123], v[142:143]
	s_nop 1
	v_permlane32_swap_b32_e32 v120, v122
	v_permlane32_swap_b32_e32 v121, v123
	v_pk_add_f32 v[62:63], v[120:121], v[122:123]
	s_bitcmp1_b32 s4, 9
	s_cbranch_scc1 .Lslowlev_A
	s_cmp_eq_u32 s9, 0
	s_cbranch_scc1 .Llevdone_A
	s_mov_b64 exec, s[6:7]
	s_waitcnt lgkmcnt(2)
	v_pk_fma_f32 v[80:81], v[40:41], v[82:83], v[78:79] op_sel_hi:[0,1,1]
	s_waitcnt lgkmcnt(1)
	v_pk_fma_f32 v[80:81], v[40:41], v[84:85], v[80:81] op_sel_hi:[0,1,1]
	s_waitcnt lgkmcnt(0)
	v_pk_fma_f32 v[80:81], v[40:41], v[86:87], v[80:81] op_sel_hi:[0,1,1]
	ds_write_b64 v137, v[80:81]
	s_mov_b64 exec, -1
	s_cmp_lt_u32 s9, 2
	s_cbranch_scc1 .Llevdone_A
	s_mov_b32 s8, 2
.Llev_A:
	v_cmp_eq_u32_e64 s[6:7], s8, v117
	s_add_u32 s8, s8, 1
	s_mov_b64 exec, s[6:7]
	ds_read_b64 v[82:83], v118
	ds_read_b64 v[84:85], v119
	ds_read_b64 v[86:87], v136
	s_waitcnt lgkmcnt(2)
	v_pk_fma_f32 v[80:81], v[40:41], v[82:83], v[78:79] op_sel_hi:[0,1,1]
	s_waitcnt lgkmcnt(1)
	v_pk_fma_f32 v[80:81], v[40:41], v[84:85], v[80:81] op_sel_hi:[0,1,1]
	s_waitcnt lgkmcnt(0)
	v_pk_fma_f32 v[80:81], v[40:41], v[86:87], v[80:81] op_sel_hi:[0,1,1]
	ds_write_b64 v137, v[80:81]
	s_mov_b64 exec, -1
	s_cmp_le_u32 s8, s9
	s_cbranch_scc1 .Llev_A
.Llevdone_A:
	s_waitcnt lgkmcnt(0)
	v_or_b32_e32 v60, v60, v61
	v_add_u32_e32 v138, 0xfffffe00, v138
	v_add_u32_e32 v139, 0xffffff00, v139
	v_add_u32_e32 v156, 0xfffffa00, v156
	v_add_u32_e32 v157, -4, v157
	v_add_u32_e32 v137, 0xfffffe00, v137
	v_max_i32_e32 v138, v138, v160
	v_max_i32_e32 v139, v139, v161
	v_max_i32_e32 v156, v156, v162
	v_max_i32_e32 v157, v157, v163
	v_lshl_add_u64 v[158:159], v[158:159], 0, s[2:3]
	v_readfirstlane_b32 s4, v60
	s_sub_u32 s5, s5, 1
.Lit_B:
	v_add_u32_sdwa v88, v116, v50 dst_sel:DWORD dst_unused:UNUSED_PAD src0_sel:DWORD src1_sel:WORD_0
	v_add_u32_sdwa v89, v116, v50 dst_sel:DWORD dst_unused:UNUSED_PAD src0_sel:DWORD src1_sel:WORD_1
	ds_read_b64 v[68:69], v88
	v_add_u32_sdwa v90, v116, v51 dst_sel:DWORD dst_unused:UNUSED_PAD src0_sel:DWORD src1_sel:WORD_0
	ds_read_b64 v[70:71], v89
	v_add_u32_sdwa v91, v116, v51 dst_sel:DWORD dst_unused:UNUSED_PAD src0_sel:DWORD src1_sel:WORD_1
	ds_read_b64 v[72:73], v90
	ds_read_b64 v[74:75], v91
	v_add_u32_sdwa v92, v105, v56 dst_sel:DWORD dst_unused:UNUSED_PAD src0_sel:DWORD src1_sel:WORD_0
	v_add_u32_sdwa v93, v105, v56 dst_sel:DWORD dst_unused:UNUSED_PAD src0_sel:DWORD src1_sel:WORD_1
	v_add_u32_sdwa v106, v105, v57 dst_sel:DWORD dst_unused:UNUSED_PAD src0_sel:DWORD src1_sel:WORD_0
	v_add_u32_sdwa v107, v105, v57 dst_sel:DWORD dst_unused:UNUSED_PAD src0_sel:DWORD src1_sel:WORD_1
	v_add_u32_sdwa v108, v105, v58 dst_sel:DWORD dst_unused:UNUSED_PAD src0_sel:DWORD src1_sel:WORD_0
	v_add_u32_sdwa v109, v105, v58 dst_sel:DWORD dst_unused:UNUSED_PAD src0_sel:DWORD src1_sel:WORD_1
	v_add_u32_sdwa v88, v105, v59 dst_sel:DWORD dst_unused:UNUSED_PAD src0_sel:DWORD src1_sel:WORD_0
	v_add_u32_sdwa v89, v105, v59 dst_sel:DWORD dst_unused:UNUSED_PAD src0_sel:DWORD src1_sel:WORD_1
	ds_read_b128 v[120:123], v92
	ds_read_b128 v[124:127], v93
	ds_read_b128 v[128:131], v106
	ds_read_b128 v[132:135], v107
	ds_read_b128 v[140:143], v108
	ds_read_b128 v[144:147], v109
	ds_read_b128 v[148:151], v88
	ds_read_b128 v[152:155], v89
	v_bfe_u32 v117, v49, 16, 7
	v_add_u32_sdwa v118, v116, v47 dst_sel:DWORD dst_unused:UNUSED_PAD src0_sel:DWORD src1_sel:WORD_0
	v_add_u32_sdwa v119, v116, v47 dst_sel:DWORD dst_unused:UNUSED_PAD src0_sel:DWORD src1_sel:WORD_1
	v_add_u32_sdwa v136, v116, v49 dst_sel:DWORD dst_unused:UNUSED_PAD src0_sel:DWORD src1_sel:WORD_0
	s_waitcnt lgkmcnt(11)
	v_pk_add_f32 v[76:77], v[62:63], v[68:69]
	s_waitcnt lgkmcnt(9)
	v_pk_add_f32 v[78:79], v[70:71], v[72:73]
	s_waitcnt lgkmcnt(8)
	v_pk_add_f32 v[76:77], v[76:77], v[74:75]
	s_nop 0
	v_pk_add_f32 v[76:77], v[76:77], v[78:79]
	s_bitcmp1_b32 s21, 10
	s_cbranch_scc1 .Lnearslow_B
.Lnearslow_ret_B:
	v_cmp_eq_u32_e32 vcc, 0, v117
	v_pk_mul_f32 v[78:79], v[48:49], v[76:77] op_sel_hi:[0,1]
	s_mov_b64 exec, vcc
	ds_write_b64 v137, v[78:79]
	s_mov_b64 exec, -1
	ds_read_b128 v[38:41], v138 offset:57408
	ds_read_b64 v[42:43], v139
	ds_read2_b64 v[52:55], v156 offset1:2
	ds_read2_b32 v[60:61], v157 offset1:16
	s_and_b32 s9, s21, 0xff
	s_waitcnt lgkmcnt(4)
	s_bitcmp1_b32 s21, 9
	s_cbranch_scc1 .Lfs_B
	s_cmp_eq_u32 s9, 0
	s_cbranch_scc1 .Lfs_B
	v_cmp_eq_u32_e64 s[6:7], 1, v117
	s_mov_b64 exec, s[6:7]
	ds_read_b64 v[82:83], v118
	ds_read_b64 v[84:85], v119
	ds_read_b64 v[86:87], v136
	s_mov_b64 exec, -1
.Lfs_B:
	v_pk_add_f32 v[120:121], v[120:121], v[124:125]
	v_pk_add_f32 v[122:123], v[122:123], v[126:127]
	v_pk_add_f32 v[128:129], v[128:129], v[132:133]
	v_pk_add_f32 v[130:131], v[130:131], v[134:135]
	v_pk_add_f32 v[140:141], v[140:141], v[144:145]
	v_pk_add_f32 v[142:143], v[142:143], v[146:147]
	v_pk_add_f32 v[148:149], v[148:149], v[152:153]
	v_pk_add_f32 v[150:151], v[150:151], v[154:155]
	s_bitcmp1_b32 s4, 8
	s_cbranch_scc1 .Lfarslow_B
.Lfarslow_ret_B:
	v_pk_add_f32 v[120:121], v[120:121], v[128:129]
	v_pk_add_f32 v[122:123], v[122:123], v[130:131]
	v_pk_add_f32 v[140:141], v[140:141], v[148:149]
	v_pk_add_f32 v[142:143], v[142:143], v[150:151]
	v_pk_add_f32 v[120:121], v[120:121], v[140:141]
	v_pk_add_f32 v[122:123], v[122:123], v[142:143]
	s_nop 1
	v_permlane32_swap_b32_e32 v120, v122
	v_permlane32_swap_b32_e32 v121, v123
	v_pk_add_f32 v[44:45], v[120:121], v[122:123]
	s_bitcmp1_b32 s21, 9
	s_cbranch_scc1 .Lslowlev_B
	s_cmp_eq_u32 s9, 0
	s_cbranch_scc1 .Llevdone_B
	s_mov_b64 exec, s[6:7]
	s_waitcnt lgkmcnt(2)
	v_pk_fma_f32 v[80:81], v[48:49], v[82:83], v[78:79] op_sel_hi:[0,1,1]
	s_waitcnt lgkmcnt(1)
	v_pk_fma_f32 v[80:81], v[48:49], v[84:85], v[80:81] op_sel_hi:[0,1,1]
	s_waitcnt lgkmcnt(0)
	v_pk_fma_f32 v[80:81], v[48:49], v[86:87], v[80:81] op_sel_hi:[0,1,1]
	ds_write_b64 v137, v[80:81]
	s_mov_b64 exec, -1
	s_cmp_lt_u32 s9, 2
	s_cbranch_scc1 .Llevdone_B
	s_mov_b32 s8, 2
.Llev_B:
	v_cmp_eq_u32_e64 s[6:7], s8, v117
	s_add_u32 s8, s8, 1
	s_mov_b64 exec, s[6:7]
	ds_read_b64 v[82:83], v118
	ds_read_b64 v[84:85], v119
	ds_read_b64 v[86:87], v136
	s_waitcnt lgkmcnt(2)
	v_pk_fma_f32 v[80:81], v[48:49], v[82:83], v[78:79] op_sel_hi:[0,1,1]
	s_waitcnt lgkmcnt(1)
	v_pk_fma_f32 v[80:81], v[48:49], v[84:85], v[80:81] op_sel_hi:[0,1,1]
	s_waitcnt lgkmcnt(0)
	v_pk_fma_f32 v[80:81], v[48:49], v[86:87], v[80:81] op_sel_hi:[0,1,1]
	ds_write_b64 v137, v[80:81]
	s_mov_b64 exec, -1
	s_cmp_le_u32 s8, s9
	s_cbranch_scc1 .Llev_B
.Llevdone_B:
	s_waitcnt lgkmcnt(0)
	v_or_b32_e32 v60, v60, v61
	v_add_u32_e32 v138, 0xfffffe00, v138
	v_add_u32_e32 v139, 0xffffff00, v139
	v_add_u32_e32 v156, 0xfffffa00, v156
	v_add_u32_e32 v157, -4, v157
	v_add_u32_e32 v137, 0xfffffe00, v137
	v_max_i32_e32 v138, v138, v160
	v_max_i32_e32 v139, v139, v161
	v_max_i32_e32 v156, v156, v162
	v_max_i32_e32 v157, v157, v163
	v_lshl_add_u64 v[158:159], v[158:159], 0, s[2:3]
	v_readfirstlane_b32 s21, v60
	s_cmp_eq_u32 s5, 0
	s_cbranch_scc1 .Lchain_done
	s_sub_u32 s5, s5, 1
	s_branch .Lchain_top
.Lfarslow_pre:
	s_waitcnt lgkmcnt(0)
	ds_read_b64 v[90:91], v156 offset:1568
	v_and_b32_e32 v164, 0x3ff, v38
	v_mov_b64_e32 v[166:167], v[158:159]
	s_movk_i32 s22, 24
	s_waitcnt lgkmcnt(0)
.Lfs_gather_pre:
	v_add_u32_sdwa v92, v105, v90 dst_sel:DWORD dst_unused:UNUSED_PAD src0_sel:DWORD src1_sel:WORD_0
	v_add_u32_sdwa v93, v105, v90 dst_sel:DWORD dst_unused:UNUSED_PAD src0_sel:DWORD src1_sel:WORD_1
	v_add_u32_sdwa v106, v105, v91 dst_sel:DWORD dst_unused:UNUSED_PAD src0_sel:DWORD src1_sel:WORD_0
	v_add_u32_sdwa v107, v105, v91 dst_sel:DWORD dst_unused:UNUSED_PAD src0_sel:DWORD src1_sel:WORD_1
	ds_read_b128 v[124:127], v92
	ds_read_b128 v[132:135], v93
	ds_read_b128 v[144:147], v106
	ds_read_b128 v[152:155], v107
	s_waitcnt lgkmcnt(0)
	v_pk_add_f32 v[124:125], v[124:125], v[132:133]
	v_pk_add_f32 v[126:127], v[126:127], v[134:135]
	v_pk_add_f32 v[144:145], v[144:145], v[152:153]
	v_pk_add_f32 v[146:147], v[146:147], v[154:155]
	v_pk_add_f32 v[124:125], v[124:125], v[144:145]
	v_pk_add_f32 v[126:127], v[126:127], v[146:147]
	s_nop 0
	v_pk_add_f32 v[148:149], v[148:149], v[124:125]
	v_pk_add_f32 v[150:151], v[150:151], v[126:127]
	v_cmp_lt_u32_e32 vcc, s22, v164
	s_cbranch_vccz .Lfarslow_ret_pre
	v_add_u32_e32 v165, s22, v112
	v_cmp_lt_u32_e32 vcc, v165, v164
	v_mov_b32_e32 v90, 0x20002000
	v_mov_b32_e32 v91, 0x20002000
	s_and_saveexec_b64 s[12:13], vcc
	global_load_dwordx2 v[90:91], v[166:167], off
	s_mov_b64 exec, -1
	v_lshl_add_u64 v[166:167], v[166:167], 0, 16
	s_add_i32 s22, s22, 8
	s_waitcnt vmcnt(0)
	s_branch .Lfs_gather_pre
.Lfarslow_A:
	s_waitcnt lgkmcnt(0)
	ds_read_b64 v[90:91], v156 offset:1568
	v_and_b32_e32 v164, 0x3ff, v46
	v_mov_b64_e32 v[166:167], v[158:159]
	s_movk_i32 s22, 24
	s_waitcnt lgkmcnt(0)

.Lnearslow_A:
	v_sub_u32_e32 v164, v137, v116
	v_lshrrev_b32_e32 v164, 2, v164
	v_add_u32_e32 v164, 0x128c0, v164
	ds_read_b32 v165, v164
	v_lshlrev_b32_e32 v166, 4, v111
	v_sub_u32_e32 v166, v137, v166
	v_add_u32_e32 v166, 0x200, v166
	s_waitcnt lgkmcnt(0)
	v_cmp_ne_u32_e32 vcc, 0, v165
	s_and_saveexec_b64 s[12:13], vcc
	s_cbranch_execz .Lnearslow_end_A
.Lnearslow_loop_A:
	v_ffbl_b32_e32 v167, v165
	v_lshl_add_u32 v167, v167, 4, v166
	ds_read_b64 v[90:91], v167
	v_add_u32_e32 v164, -1, v165
	v_and_b32_e32 v165, v164, v165
	s_waitcnt lgkmcnt(0)
	v_pk_add_f32 v[76:77], v[76:77], v[90:91]
	v_cmp_ne_u32_e32 vcc, 0, v165
	s_and_b64 exec, exec, vcc
	s_cbranch_execnz .Lnearslow_loop_A
.Lnearslow_end_A:
	s_mov_b64 exec, -1
	s_branch .Lnearslow_ret_A

.Lslowlev_A:
	s_waitcnt lgkmcnt(0)
	s_mov_b32 s8, 1
	v_sub_u32_e32 v164, v137, v116
	v_lshrrev_b32_e32 v164, 2, v164
	v_add_u32_e32 v164, 0x11040, v164
	v_lshlrev_b32_e32 v166, 4, v111
	v_sub_u32_e32 v166, v137, v166
	v_and_b32_e32 v165, 0x800000, v41
.Lsl_A:
	v_cmp_eq_u32_e64 s[6:7], s8, v117
	s_add_u32 s8, s8, 1
	s_mov_b64 exec, s[6:7]
	ds_read_b64 v[82:83], v118
	ds_read_b64 v[84:85], v119
	ds_read_b64 v[86:87], v136
	s_waitcnt lgkmcnt(2)
	v_pk_fma_f32 v[80:81], v[40:41], v[82:83], v[78:79] op_sel_hi:[0,1,1]
	s_waitcnt lgkmcnt(1)
	v_pk_fma_f32 v[80:81], v[40:41], v[84:85], v[80:81] op_sel_hi:[0,1,1]
	s_waitcnt lgkmcnt(0)
	v_pk_fma_f32 v[80:81], v[40:41], v[86:87], v[80:81] op_sel_hi:[0,1,1]
	v_cmp_ne_u32_e32 vcc, 0, v165
	s_and_saveexec_b64 s[12:13], vcc
	s_cbranch_execz .Lsl_w_A
	ds_read_b32 v167, v164
	s_waitcnt lgkmcnt(0)
.Lsl_in_A:
	v_ffbl_b32_e32 v88, v167
	v_lshl_add_u32 v88, v88, 4, v166
	ds_read_b64 v[90:91], v88
	v_add_u32_e32 v89, -1, v167
	v_and_b32_e32 v167, v89, v167
	s_waitcnt lgkmcnt(0)
	v_pk_fma_f32 v[80:81], v[40:41], v[90:91], v[80:81] op_sel_hi:[0,1,1]
	v_cmp_ne_u32_e32 vcc, 0, v167
	s_and_b64 exec, exec, vcc
	s_cbranch_execnz .Lsl_in_A
.Lsl_w_A:
	s_mov_b64 exec, s[6:7]
	ds_write_b64 v137, v[80:81]
	s_mov_b64 exec, -1
	s_cmp_le_u32 s8, s9
	s_cbranch_scc1 .Lsl_A
	s_branch .Llevdone_A
.Lslowlev_B:
	s_waitcnt lgkmcnt(0)
	s_mov_b32 s8, 1
	v_sub_u32_e32 v164, v137, v116
	v_lshrrev_b32_e32 v164, 2, v164
	v_add_u32_e32 v164, 0x11040, v164
	v_lshlrev_b32_e32 v166, 4, v111
	v_sub_u32_e32 v166, v137, v166
	v_and_b32_e32 v165, 0x800000, v49
.Lsl_B:
	v_cmp_eq_u32_e64 s[6:7], s8, v117
	s_add_u32 s8, s8, 1
	s_mov_b64 exec, s[6:7]
	ds_read_b64 v[82:83], v118
	ds_read_b64 v[84:85], v119
	ds_read_b64 v[86:87], v136
	s_waitcnt lgkmcnt(2)
	v_pk_fma_f32 v[80:81], v[48:49], v[82:83], v[78:79] op_sel_hi:[0,1,1]
	s_waitcnt lgkmcnt(1)
	v_pk_fma_f32 v[80:81], v[48:49], v[84:85], v[80:81] op_sel_hi:[0,1,1]
	s_waitcnt lgkmcnt(0)
	v_pk_fma_f32 v[80:81], v[48:49], v[86:87], v[80:81] op_sel_hi:[0,1,1]
	v_cmp_ne_u32_e32 vcc, 0, v165
	s_and_saveexec_b64 s[12:13], vcc
	s_cbranch_execz .Lsl_w_B
	ds_read_b32 v167, v164
	s_waitcnt lgkmcnt(0)
.Lsl_in_B:
	v_ffbl_b32_e32 v88, v167
	v_lshl_add_u32 v88, v88, 4, v166
	ds_read_b64 v[90:91], v88
	v_add_u32_e32 v89, -1, v167
	v_and_b32_e32 v167, v89, v167
	s_waitcnt lgkmcnt(0)
	v_pk_fma_f32 v[80:81], v[48:49], v[90:91], v[80:81] op_sel_hi:[0,1,1]
	v_cmp_ne_u32_e32 vcc, 0, v167
	s_and_b64 exec, exec, vcc
	s_cbranch_execnz .Lsl_in_B

.Lchain_done:
.LBB2_44:
	v_mov_b32_e32 v0, 0x10040
	v_lshl_or_b32 v54, v1, 4, v0
	v_lshl_add_u32 v0, v110, 6, v54
	v_add_u32_e32 v55, 0x4c, v67
	s_waitcnt vmcnt(8)
	ds_write_b128 v0, v[34:37]
	s_waitcnt lgkmcnt(0)
	s_barrier
	ds_read2st64_b32 v[0:1], v55 offset0:224 offset1:228
	s_add_u32 s0, s16, s18
	s_addc_u32 s1, s17, s19
	v_lshl_add_u64 v[50:51], v[98:99], 4, s[0:1]
	v_mul_u32_u24_e32 v38, 0xc00, v110
	s_waitcnt lgkmcnt(0)
	v_lshrrev_b32_e32 v0, 24, v0
	v_lshl_add_u32 v0, v0, 6, v54
	v_mov_b32_e32 v39, 0
	ds_read_b128 v[34:37], v66
	v_lshl_add_u64 v[52:53], v[50:51], 0, v[38:39]
	ds_read_b128 v[38:41], v0
	ds_read_b128 v[42:45], v66 offset:1024
	v_lshrrev_b32_e32 v0, 24, v1
	v_lshl_add_u32 v0, v0, 6, v54
	ds_read_b128 v[46:49], v0
	s_waitcnt vmcnt(7) lgkmcnt(3)
	v_pk_add_f32 v[30:31], v[34:35], v[30:31]
	v_pk_add_f32 v[0:1], v[36:37], v[32:33]
	s_waitcnt vmcnt(6) lgkmcnt(1)
	v_pk_add_f32 v[26:27], v[42:43], v[26:27]
	v_pk_add_f32 v[28:29], v[44:45], v[28:29]
	v_pk_add_f32 v[30:31], v[30:31], v[38:39]
	v_pk_add_f32 v[32:33], v[0:1], v[40:41]
	v_lshl_add_u64 v[0:1], v[50:51], 0, v[102:103]
	s_waitcnt lgkmcnt(0)
	v_pk_add_f32 v[26:27], v[26:27], v[46:47]
	ds_read2st64_b32 v[38:39], v55 offset0:232 offset1:236
	v_pk_add_f32 v[28:29], v[28:29], v[48:49]
	global_store_dwordx4 v[52:53], v[30:33], off
	global_store_dwordx4 v[0:1], v[26:29], off
	ds_read_b128 v[26:29], v66 offset:2048
	s_waitcnt lgkmcnt(1)
	v_lshrrev_b32_e32 v30, 24, v38
	v_lshl_add_u32 v30, v30, 6, v54
	ds_read_b128 v[30:33], v30
	ds_read_b128 v[34:37], v66 offset:3072
	s_mov_b32 s0, 0x30000
	s_waitcnt vmcnt(7) lgkmcnt(2)
	v_pk_add_f32 v[22:23], v[26:27], v[22:23]
	v_lshrrev_b32_e32 v26, 24, v39
	v_lshl_add_u32 v26, v26, 6, v54
	ds_read_b128 v[38:41], v26
	v_add_co_u32_e32 v26, vcc, s0, v0
	s_mov_b32 s0, 0x60000
	s_nop 0
	v_addc_co_u32_e32 v27, vcc, 0, v1, vcc
	s_waitcnt lgkmcnt(2)
	v_pk_add_f32 v[22:23], v[22:23], v[30:31]
	s_waitcnt vmcnt(6) lgkmcnt(1)
	v_pk_add_f32 v[18:19], v[34:35], v[18:19]
	v_pk_add_f32 v[20:21], v[36:37], v[20:21]
	ds_read2st64_b32 v[30:31], v55 offset0:240 offset1:244
	v_add_co_u32_e32 v0, vcc, s0, v0
	s_waitcnt lgkmcnt(1)
	v_pk_add_f32 v[18:19], v[18:19], v[38:39]
	v_pk_add_f32 v[20:21], v[20:21], v[40:41]
	v_addc_co_u32_e32 v1, vcc, 0, v1, vcc
	global_store_dwordx4 v[0:1], v[18:21], off
	ds_read_b128 v[18:21], v66 offset:4096
	v_pk_add_f32 v[24:25], v[28:29], v[24:25]
	s_waitcnt lgkmcnt(1)
	v_lshrrev_b32_e32 v0, 24, v30
	v_pk_add_f32 v[24:25], v[24:25], v[32:33]
	global_store_dwordx4 v[26:27], v[22:25], off
	v_lshl_add_u32 v0, v0, 6, v54
	ds_read_b128 v[22:25], v0
	ds_read_b128 v[26:29], v66 offset:5120
	s_waitcnt vmcnt(7) lgkmcnt(2)
	v_pk_add_f32 v[0:1], v[18:19], v[14:15]
	v_lshrrev_b32_e32 v14, 24, v31
	v_lshl_add_u32 v14, v14, 6, v54
	ds_read_b128 v[30:33], v14
	s_waitcnt lgkmcnt(2)
	v_pk_add_f32 v[14:15], v[0:1], v[22:23]
	v_pk_add_f32 v[0:1], v[20:21], v[16:17]
	s_mov_b32 s0, 0xc0000
	v_pk_add_f32 v[16:17], v[0:1], v[24:25]
	v_add_co_u32_e32 v0, vcc, s0, v52
	s_waitcnt vmcnt(6) lgkmcnt(1)
	v_pk_add_f32 v[10:11], v[26:27], v[10:11]
	v_addc_co_u32_e32 v1, vcc, 0, v53, vcc
	v_pk_add_f32 v[12:13], v[28:29], v[12:13]
	global_store_dwordx4 v[0:1], v[14:17], off
	v_lshl_add_u64 v[0:1], v[50:51], 0, v[100:101]
	ds_read2st64_b32 v[22:23], v55 offset0:248 offset1:252
	s_waitcnt lgkmcnt(1)
	v_pk_add_f32 v[10:11], v[10:11], v[30:31]
	v_pk_add_f32 v[12:13], v[12:13], v[32:33]
	global_store_dwordx4 v[0:1], v[10:13], off
	ds_read_b128 v[10:13], v66 offset:6144
	s_waitcnt lgkmcnt(1)
	v_lshrrev_b32_e32 v0, 24, v22
	v_lshl_add_u32 v14, v0, 6, v54
	ds_read_b128 v[14:17], v14
	ds_read_b128 v[18:21], v66 offset:7168
	v_lshl_add_u64 v[0:1], v[50:51], 0, v[96:97]
	s_waitcnt vmcnt(7) lgkmcnt(2)
	v_pk_add_f32 v[6:7], v[10:11], v[6:7]
	v_lshrrev_b32_e32 v10, 24, v23
	v_lshl_add_u32 v10, v10, 6, v54
	ds_read_b128 v[22:25], v10
	v_pk_add_f32 v[8:9], v[12:13], v[8:9]
	s_waitcnt lgkmcnt(2)
	v_pk_add_f32 v[6:7], v[6:7], v[14:15]
	v_pk_add_f32 v[8:9], v[8:9], v[16:17]
	global_store_dwordx4 v[0:1], v[6:9], off
	s_waitcnt vmcnt(7) lgkmcnt(1)
	v_pk_add_f32 v[0:1], v[18:19], v[2:3]
	v_pk_add_f32 v[2:3], v[20:21], v[4:5]
	v_lshl_add_u64 v[6:7], v[50:51], 0, v[94:95]
	s_waitcnt lgkmcnt(0)
	v_pk_add_f32 v[0:1], v[0:1], v[22:23]
	v_pk_add_f32 v[2:3], v[2:3], v[24:25]
	global_store_dwordx4 v[6:7], v[0:3], off
	s_endpgm

	.amdhsa_kernel _Z8k3_chainPKfPK15HIP_vector_typeIiLj4EEPKtS6_S0_S0_Pf
		.amdhsa_group_segment_fixed_size 78016
		.amdhsa_private_segment_fixed_size 0
		.amdhsa_kernarg_size 56
		.amdhsa_user_sgpr_count 2
		.amdhsa_user_sgpr_dispatch_ptr 0
		.amdhsa_user_sgpr_queue_ptr 0
		.amdhsa_user_sgpr_kernarg_segment_ptr 1
		.amdhsa_user_sgpr_dispatch_id 0
		.amdhsa_user_sgpr_kernarg_preload_length 0
		.amdhsa_user_sgpr_kernarg_preload_offset 0
		.amdhsa_user_sgpr_private_segment_size 0
		.amdhsa_uses_dynamic_stack 0
		.amdhsa_enable_private_segment 0
		.amdhsa_system_sgpr_workgroup_id_x 1
		.amdhsa_system_sgpr_workgroup_id_y 0
		.amdhsa_system_sgpr_workgroup_id_z 0
		.amdhsa_system_sgpr_workgroup_info 0
		.amdhsa_system_vgpr_workitem_id 0
		.amdhsa_next_free_vgpr 169
		.amdhsa_next_free_sgpr 96
		.amdhsa_accum_offset 168
		.amdhsa_reserve_vcc 1
		.amdhsa_float_round_mode_32 0
		.amdhsa_float_round_mode_16_64 0
		.amdhsa_float_denorm_mode_32 3
		.amdhsa_float_denorm_mode_16_64 3
		.amdhsa_dx10_clamp 1
		.amdhsa_ieee_mode 1
		.amdhsa_fp16_overflow 0
		.amdhsa_tg_split 0
		.amdhsa_exception_fp_ieee_invalid_op 0
		.amdhsa_exception_fp_denorm_src 0
		.amdhsa_exception_fp_ieee_div_zero 0
		.amdhsa_exception_fp_ieee_overflow 0
		.amdhsa_exception_fp_ieee_underflow 0
		.amdhsa_exception_fp_ieee_inexact 0
		.amdhsa_exception_int_div_zero 0
	.end_amdhsa_kernel

amdhsa.kernels:
  - .agpr_count:     0
    .args:
      - .actual_access:  read_only
        .address_space:  global
        .offset:         0
        .size:           8
        .value_kind:     global_buffer
      - .actual_access:  read_only
        .address_space:  global
        .offset:         8
        .size:           8
        .value_kind:     global_buffer
      - .actual_access:  write_only
        .address_space:  global
        .offset:         16
        .size:           8
        .value_kind:     global_buffer
      - .actual_access:  write_only
        .address_space:  global
        .offset:         24
        .size:           8
        .value_kind:     global_buffer
      - .actual_access:  write_only
        .address_space:  global
        .offset:         32
        .size:           8
        .value_kind:     global_buffer
    .group_segment_fixed_size: 1024
    .kernarg_segment_align: 8
    .kernarg_segment_size: 40
    .language:       OpenCL C
    .language_version:
      - 2
      - 0
    .max_flat_workgroup_size: 256
    .name:           _Z7k1_packPKfS0_PmPiP15HIP_vector_typeIfLj4EE
    .private_segment_fixed_size: 0
    .sgpr_count:     16
    .sgpr_spill_count: 0
    .symbol:         _Z7k1_packPKfS0_PmPiP15HIP_vector_typeIfLj4EE.kd
    .uniform_work_group_size: 1
    .uses_dynamic_stack: false
    .vgpr_count:     33
    .vgpr_spill_count: 0
    .wavefront_size: 64
  - .agpr_count:     0
    .args:
      - .actual_access:  read_only
        .address_space:  global
        .offset:         0
        .size:           8
        .value_kind:     global_buffer
      - .actual_access:  read_only
        .address_space:  global
        .offset:         8
        .size:           8
        .value_kind:     global_buffer
      - .actual_access:  write_only
        .address_space:  global
        .offset:         16
        .size:           8
        .value_kind:     global_buffer
      - .actual_access:  read_only
        .address_space:  global
        .offset:         24
        .size:           8
        .value_kind:     global_buffer
      - .actual_access:  write_only
        .address_space:  global
        .offset:         32
        .size:           8
        .value_kind:     global_buffer
      - .actual_access:  write_only
        .address_space:  global
        .offset:         40
        .size:           8
        .value_kind:     global_buffer
      - .actual_access:  read_only
        .address_space:  global
        .offset:         48
        .size:           8
        .value_kind:     global_buffer
      - .address_space:  global
        .offset:         56
        .size:           8
        .value_kind:     global_buffer
      - .actual_access:  write_only
        .address_space:  global
        .offset:         64
        .size:           8
        .value_kind:     global_buffer
      - .actual_access:  write_only
        .address_space:  global
        .offset:         72
        .size:           8
        .value_kind:     global_buffer
    .group_segment_fixed_size: 34880
    .kernarg_segment_align: 8
    .kernarg_segment_size: 80
    .language:       OpenCL C
    .language_version:
      - 2
      - 0
    .max_flat_workgroup_size: 512
    .name:           _Z7k2_elimPKjPKiPiS2_PfP15HIP_vector_typeIiLj4EEPKfS4_PtSA_
    .private_segment_fixed_size: 0
    .sgpr_count:     50
    .sgpr_spill_count: 0
    .symbol:         _Z7k2_elimPKjPKiPiS2_PfP15HIP_vector_typeIiLj4EEPKfS4_PtSA_.kd
    .uniform_work_group_size: 1
    .uses_dynamic_stack: false
    .vgpr_count:     35
    .vgpr_spill_count: 0
    .wavefront_size: 64
  - .agpr_count:     0
    .args:
      - .actual_access:  read_only
        .address_space:  global
        .offset:         0
        .size:           8
        .value_kind:     global_buffer
      - .actual_access:  read_only
        .address_space:  global
        .offset:         8
        .size:           8
        .value_kind:     global_buffer
      - .actual_access:  read_only
        .address_space:  global
        .offset:         16
        .size:           8
        .value_kind:     global_buffer
      - .actual_access:  read_only
        .address_space:  global
        .offset:         24
        .size:           8
        .value_kind:     global_buffer
      - .actual_access:  read_only
        .address_space:  global
        .offset:         32
        .size:           8
        .value_kind:     global_buffer
      - .actual_access:  read_only
        .address_space:  global
        .offset:         40
        .size:           8
        .value_kind:     global_buffer
      - .actual_access:  write_only
        .address_space:  global
        .offset:         48
        .size:           8
        .value_kind:     global_buffer
    .group_segment_fixed_size: 78016
    .kernarg_segment_align: 8
    .kernarg_segment_size: 56
    .language:       OpenCL C
    .language_version:
      - 2
      - 0
    .max_flat_workgroup_size: 256
    .name:           _Z8k3_chainPKfPK15HIP_vector_typeIiLj4EEPKtS6_S0_S0_Pf
    .private_segment_fixed_size: 0
    .sgpr_count:     28
    .sgpr_spill_count: 0
    .symbol:         _Z8k3_chainPKfPK15HIP_vector_typeIiLj4EEPKtS6_S0_S0_Pf.kd
    .uniform_work_group_size: 1
    .uses_dynamic_stack: false
    .vgpr_count:     168
    .vgpr_spill_count: 0
    .wavefront_size: 64
